# A-side fragment reuse (24 instead of 32 LDS fragment reads per K-tile) extended to the DOWN, UQ, ROUTER0/1 and WO1 fp8 GEMM K-loops
# speedup vs baseline: 1.0058x; 1.0058x over previous
.LBB0_220:
	s_add_u32 s40, s10, s38
	s_addc_u32 s41, s11, s39
	s_add_u32 s42, s40, 0x49800100
	ds_read_b128 v[144:147], v154
	ds_read_b128 v[170:173], v154 offset:2048
	ds_read_b128 v[148:151], v155
	ds_read_b128 v[174:177], v155 offset:2048
	s_addc_u32 s43, s41, 0
	s_add_u32 s67, s1, s38
	s_addc_u32 s68, s56, s39
	s_cmpk_eq_i32 s38, 0x700
	s_cselect_b64 vcc, -1, 0
	s_and_b64 s[40:41], vcc, exec
	v_cndmask_b32_e32 v132, v135, v165, vcc
	s_cselect_b32 s43, s13, s43
	s_cselect_b32 s42, s12, s42
	s_cselect_b32 s41, s37, s68
	s_cselect_b32 s40, s36, s67
	v_cndmask_b32_e32 v137, v136, v167, vcc
	v_lshl_add_u64 v[212:213], v[142:143], 0, s[38:39]
	s_add_i32 m0, s33, 0xc000
	ds_read_b128 v[178:181], v152
	ds_read_b128 v[186:189], v152 offset:2048
	ds_read_b128 v[182:185], v153
	ds_read_b128 v[190:193], v153 offset:2048
	ds_read_b128 v[196:199], v152 offset:4096
	ds_read_b128 v[204:207], v152 offset:6144
	ds_read_b128 v[200:203], v153 offset:4096
	ds_read_b128 v[208:211], v153 offset:6144
	global_load_lds_dwordx4 v[212:213], off
	v_lshl_add_u64 v[212:213], v[140:141], 0, s[38:39]
	s_add_i32 m0, s33, 0xe000
	v_cndmask_b32_e32 v220, v134, v166, vcc
	global_load_lds_dwordx4 v[212:213], off
	s_waitcnt lgkmcnt(8)
	s_barrier
	s_waitcnt lgkmcnt(0)
	s_setprio 1
	s_waitcnt lgkmcnt(0)
	v_mfma_f32_16x16x128_f8f6f4 v[124:127], v[144:151], v[178:185], v[124:127]
	v_mfma_f32_16x16x128_f8f6f4 v[120:123], v[170:177], v[178:185], v[120:123]
	v_mfma_f32_16x16x128_f8f6f4 v[108:111], v[144:151], v[186:193], v[108:111]
	v_mfma_f32_16x16x128_f8f6f4 v[104:107], v[170:177], v[186:193], v[104:107]
	v_mfma_f32_16x16x128_f8f6f4 v[92:95], v[144:151], v[196:203], v[92:95]
	v_mfma_f32_16x16x128_f8f6f4 v[88:91], v[170:177], v[196:203], v[88:91]
	v_mfma_f32_16x16x128_f8f6f4 v[76:79], v[144:151], v[204:211], v[76:79]
	v_mfma_f32_16x16x128_f8f6f4 v[72:75], v[170:177], v[204:211], v[72:75]
	s_setprio 0
	s_barrier
	ds_read_b128 v[222:225], v154 offset:16384
	ds_read_b128 v[230:233], v154 offset:18432
	ds_read_b128 v[226:229], v155 offset:16384
	ds_read_b128 v[234:237], v155 offset:18432
	s_barrier
	s_waitcnt lgkmcnt(0)
	s_setprio 1
	s_waitcnt lgkmcnt(0)
	v_mfma_f32_16x16x128_f8f6f4 v[116:119], v[222:229], v[178:185], v[116:119]
	v_mfma_f32_16x16x128_f8f6f4 v[112:115], v[230:237], v[178:185], v[112:115]
	v_mfma_f32_16x16x128_f8f6f4 v[100:103], v[222:229], v[186:193], v[100:103]
	v_mfma_f32_16x16x128_f8f6f4 v[96:99], v[230:237], v[186:193], v[96:99]
	v_mfma_f32_16x16x128_f8f6f4 v[84:87], v[222:229], v[196:203], v[84:87]
	v_mfma_f32_16x16x128_f8f6f4 v[80:83], v[230:237], v[196:203], v[80:83]
	v_mfma_f32_16x16x128_f8f6f4 v[68:71], v[222:229], v[204:211], v[68:71]
	v_mfma_f32_16x16x128_f8f6f4 v[64:67], v[230:237], v[204:211], v[64:67]
	s_setprio 0
	s_barrier
	s_mov_b32 m0, s33
	ds_read_b128 v[186:189], v152 offset:16384
	ds_read_b128 v[196:199], v152 offset:18432
	ds_read_b128 v[190:193], v153 offset:16384
	ds_read_b128 v[200:203], v153 offset:18432
	ds_read_b128 v[204:207], v152 offset:20480
	ds_read_b128 v[212:215], v152 offset:22528
	ds_read_b128 v[208:211], v153 offset:20480
	ds_read_b128 v[216:219], v153 offset:22528
	global_load_lds_dwordx4 v132, s[42:43]
	s_mov_b32 m0, s46
	v_mov_b32_e32 v221, v133
	global_load_lds_dwordx4 v220, s[42:43]
	s_waitcnt lgkmcnt(8)
	s_barrier
	s_waitcnt lgkmcnt(0)
	v_lshl_add_u64 v[246:247], s[42:43], 0, v[132:133]
	v_lshl_add_u64 v[244:245], s[42:43], 0, v[220:221]
	s_setprio 1
	s_waitcnt lgkmcnt(0)
	v_mfma_f32_16x16x128_f8f6f4 v[60:63], v[144:151], v[186:193], v[60:63]
	v_mfma_f32_16x16x128_f8f6f4 v[56:59], v[170:177], v[186:193], v[56:59]
	v_mfma_f32_16x16x128_f8f6f4 v[44:47], v[144:151], v[196:203], v[44:47]
	v_mfma_f32_16x16x128_f8f6f4 v[40:43], v[170:177], v[196:203], v[40:43]
	v_mfma_f32_16x16x128_f8f6f4 v[28:31], v[144:151], v[204:211], v[28:31]
	v_mfma_f32_16x16x128_f8f6f4 v[24:27], v[170:177], v[204:211], v[24:27]
	v_mfma_f32_16x16x128_f8f6f4 v[12:15], v[144:151], v[212:219], v[12:15]
	v_mfma_f32_16x16x128_f8f6f4 v[8:11], v[170:177], v[212:219], v[8:11]
	s_setprio 0
	s_barrier
	s_mov_b32 m0, s44
	v_lshl_add_u64 v[144:145], s[40:41], 0, v[128:129]
	global_load_lds_dwordx4 v[144:145], off
	v_lshl_add_u64 v[146:147], s[40:41], 0, v[130:131]
	s_mov_b32 m0, s45
	s_nop 0
	global_load_lds_dwordx4 v[146:147], off
	s_waitcnt vmcnt(4)
	s_waitcnt lgkmcnt(0)
	s_barrier
	s_setprio 1
	s_waitcnt lgkmcnt(0)
	v_mfma_f32_16x16x128_f8f6f4 v[52:55], v[222:229], v[186:193], v[52:55]
	v_mfma_f32_16x16x128_f8f6f4 v[48:51], v[230:237], v[186:193], v[48:51]
	v_mfma_f32_16x16x128_f8f6f4 v[36:39], v[222:229], v[196:203], v[36:39]
	v_mfma_f32_16x16x128_f8f6f4 v[32:35], v[230:237], v[196:203], v[32:35]
	v_mfma_f32_16x16x128_f8f6f4 v[20:23], v[222:229], v[204:211], v[20:23]
	v_mfma_f32_16x16x128_f8f6f4 v[16:19], v[230:237], v[204:211], v[16:19]
	v_mfma_f32_16x16x128_f8f6f4 v[4:7], v[222:229], v[212:219], v[4:7]
	v_mfma_f32_16x16x128_f8f6f4 v[0:3], v[230:237], v[212:219], v[0:3]
	s_setprio 0
	s_barrier
	ds_read_b128 v[170:173], v154 offset:32768
	ds_read_b128 v[178:181], v154 offset:34816
	ds_read_b128 v[174:177], v155 offset:32768
	ds_read_b128 v[182:185], v155 offset:34816
	s_mov_b32 m0, s49
	ds_read_b128 v[186:189], v152 offset:32768
	ds_read_b128 v[196:199], v152 offset:34816
	ds_read_b128 v[190:193], v153 offset:32768
	ds_read_b128 v[200:203], v153 offset:34816
	ds_read_b128 v[204:207], v152 offset:36864
	ds_read_b128 v[212:215], v152 offset:38912
	ds_read_b128 v[208:211], v153 offset:36864
	ds_read_b128 v[216:219], v153 offset:38912
	v_cndmask_b32_e32 v132, v138, v168, vcc
	global_load_lds_dwordx4 v137, s[42:43]
	s_mov_b32 m0, s50
	s_nop 0
	global_load_lds_dwordx4 v132, s[42:43]
	s_add_u32 s42, s40, 0x4000
	s_addc_u32 s43, s41, 0
	v_lshl_add_u64 v[220:221], s[42:43], 0, v[128:129]
	s_mov_b32 m0, s47
	s_nop 0
	global_load_lds_dwordx4 v[220:221], off
	v_lshl_add_u64 v[220:221], s[42:43], 0, v[130:131]
	s_mov_b32 m0, s48
	s_nop 0
	global_load_lds_dwordx4 v[220:221], off
	s_waitcnt lgkmcnt(8)
	s_barrier
	s_waitcnt lgkmcnt(0)
	s_setprio 1
	s_waitcnt lgkmcnt(0)
	v_mfma_f32_16x16x128_f8f6f4 v[124:127], v[170:177], v[186:193], v[124:127]
	v_mfma_f32_16x16x128_f8f6f4 v[120:123], v[178:185], v[186:193], v[120:123]
	v_mfma_f32_16x16x128_f8f6f4 v[108:111], v[170:177], v[196:203], v[108:111]
	v_mfma_f32_16x16x128_f8f6f4 v[104:107], v[178:185], v[196:203], v[104:107]
	v_mfma_f32_16x16x128_f8f6f4 v[92:95], v[170:177], v[204:211], v[92:95]
	v_mfma_f32_16x16x128_f8f6f4 v[88:91], v[178:185], v[204:211], v[88:91]
	v_mfma_f32_16x16x128_f8f6f4 v[76:79], v[170:177], v[212:219], v[76:79]
	v_mfma_f32_16x16x128_f8f6f4 v[72:75], v[178:185], v[212:219], v[72:75]
	s_setprio 0
	s_barrier
	ds_read_b128 v[222:225], v154 offset:49152
	ds_read_b128 v[230:233], v154 offset:51200
	ds_read_b128 v[226:229], v155 offset:49152
	ds_read_b128 v[234:237], v155 offset:51200
	s_barrier
	s_waitcnt lgkmcnt(0)
	s_setprio 1
	s_waitcnt lgkmcnt(0)
	v_mfma_f32_16x16x128_f8f6f4 v[116:119], v[222:229], v[186:193], v[116:119]
	v_mfma_f32_16x16x128_f8f6f4 v[112:115], v[230:237], v[186:193], v[112:115]
	v_mfma_f32_16x16x128_f8f6f4 v[100:103], v[222:229], v[196:203], v[100:103]
	v_mfma_f32_16x16x128_f8f6f4 v[96:99], v[230:237], v[196:203], v[96:99]
	v_mfma_f32_16x16x128_f8f6f4 v[84:87], v[222:229], v[204:211], v[84:87]
	v_mfma_f32_16x16x128_f8f6f4 v[80:83], v[230:237], v[204:211], v[80:83]
	v_mfma_f32_16x16x128_f8f6f4 v[68:71], v[222:229], v[212:219], v[68:71]
	v_mfma_f32_16x16x128_f8f6f4 v[64:67], v[230:237], v[212:219], v[64:67]
	s_setprio 0
	s_barrier
	s_mov_b32 m0, s54
	v_lshl_add_u64 v[246:247], v[246:247], 0, s[24:25]
	ds_read_b128 v[186:189], v152 offset:49152
	ds_read_b128 v[196:199], v152 offset:51200
	ds_read_b128 v[190:193], v153 offset:49152
	ds_read_b128 v[200:203], v153 offset:51200
	ds_read_b128 v[204:207], v152 offset:53248
	ds_read_b128 v[212:215], v152 offset:55296
	ds_read_b128 v[208:211], v153 offset:53248
	ds_read_b128 v[216:219], v153 offset:55296
	global_load_lds_dwordx4 v[246:247], off
	v_lshl_add_u64 v[244:245], v[244:245], 0, s[24:25]
	s_mov_b32 m0, s55
	s_nop 0
	global_load_lds_dwordx4 v[244:245], off
	s_waitcnt lgkmcnt(8)
	s_barrier
	s_waitcnt lgkmcnt(0)
	s_setprio 1
	s_waitcnt lgkmcnt(0)
	v_mfma_f32_16x16x128_f8f6f4 v[60:63], v[170:177], v[186:193], v[60:63]
	v_mfma_f32_16x16x128_f8f6f4 v[56:59], v[178:185], v[186:193], v[56:59]
	v_mfma_f32_16x16x128_f8f6f4 v[44:47], v[170:177], v[196:203], v[44:47]
	v_mfma_f32_16x16x128_f8f6f4 v[40:43], v[178:185], v[196:203], v[40:43]
	v_mfma_f32_16x16x128_f8f6f4 v[28:31], v[170:177], v[204:211], v[28:31]
	v_mfma_f32_16x16x128_f8f6f4 v[24:27], v[178:185], v[204:211], v[24:27]
	v_mfma_f32_16x16x128_f8f6f4 v[12:15], v[170:177], v[212:219], v[12:15]
	v_mfma_f32_16x16x128_f8f6f4 v[8:11], v[178:185], v[212:219], v[8:11]
	s_setprio 0
	s_barrier
	s_mov_b32 m0, s52
	v_lshl_add_u64 v[144:145], v[144:145], 0, s[24:25]
	global_load_lds_dwordx4 v[144:145], off
	v_lshl_add_u64 v[144:145], v[146:147], 0, s[24:25]
	s_mov_b32 m0, s53
	s_nop 0
	global_load_lds_dwordx4 v[144:145], off
	s_waitcnt vmcnt(4)
	s_waitcnt lgkmcnt(0)
	s_barrier
	s_setprio 1
	s_waitcnt lgkmcnt(0)
	v_mfma_f32_16x16x128_f8f6f4 v[52:55], v[222:229], v[186:193], v[52:55]
	v_mfma_f32_16x16x128_f8f6f4 v[48:51], v[230:237], v[186:193], v[48:51]
	v_mfma_f32_16x16x128_f8f6f4 v[36:39], v[222:229], v[196:203], v[36:39]
	v_mfma_f32_16x16x128_f8f6f4 v[32:35], v[230:237], v[196:203], v[32:35]
	v_mfma_f32_16x16x128_f8f6f4 v[20:23], v[222:229], v[204:211], v[20:23]
	v_mfma_f32_16x16x128_f8f6f4 v[16:19], v[230:237], v[204:211], v[16:19]
	v_mfma_f32_16x16x128_f8f6f4 v[4:7], v[222:229], v[212:219], v[4:7]
	v_mfma_f32_16x16x128_f8f6f4 v[0:3], v[230:237], v[212:219], v[0:3]
	s_setprio 0
	s_barrier
	s_add_u32 s40, s40, 0x4080
	s_addc_u32 s41, s41, 0
	s_mov_b32 m0, s58
	v_lshl_add_u64 v[144:145], s[40:41], 0, v[128:129]
	global_load_lds_dwordx4 v[144:145], off
	v_lshl_add_u64 v[144:145], s[40:41], 0, v[130:131]
	s_mov_b32 m0, s59
	s_add_i32 s57, s57, 2
	global_load_lds_dwordx4 v[144:145], off
	s_add_u32 s38, s38, 0x100
	s_addc_u32 s39, s39, 0
	s_cmp_gt_u32 s57, 13
	s_cbranch_scc0 .LBB0_220
	s_and_b64 vcc, exec, s[28:29]
	s_cbranch_vccz .LBB0_223
	s_barrier

.LBB0_313:
	s_add_u32 s36, s6, s34
	s_addc_u32 s37, s7, s35
	s_add_u32 s38, s36, 0x4e000100
	ds_read_b128 v[158:161], v167
	ds_read_b128 v[172:175], v167 offset:2048
	ds_read_b128 v[162:165], v168
	ds_read_b128 v[176:179], v168 offset:2048
	s_addc_u32 s39, s37, 0
	s_add_u32 s70, s67, s34
	s_addc_u32 s71, s68, s35
	s_cmpk_eq_i32 s34, 0x200
	s_cselect_b64 vcc, -1, 0
	s_and_b64 s[36:37], vcc, exec
	v_cndmask_b32_e32 v136, v146, v138, vcc
	s_cselect_b32 s39, s9, s39
	s_cselect_b32 s38, s8, s38
	s_cselect_b32 s37, s31, s71
	s_cselect_b32 s36, s30, s70
	v_cndmask_b32_e32 v139, v150, v142, vcc
	v_lshl_add_u64 v[188:189], v[156:157], 0, s[34:35]
	s_add_i32 m0, s46, 0xc000
	ds_read_b128 v[180:183], v129
	ds_read_b128 v[196:199], v129 offset:2048
	ds_read_b128 v[184:187], v131
	ds_read_b128 v[200:203], v131 offset:2048
	ds_read_b128 v[204:207], v129 offset:4096
	ds_read_b128 v[212:215], v129 offset:6144
	ds_read_b128 v[208:211], v131 offset:4096
	ds_read_b128 v[216:219], v131 offset:6144
	global_load_lds_dwordx4 v[188:189], off
	v_lshl_add_u64 v[188:189], v[154:155], 0, s[34:35]
	s_add_i32 m0, s46, 0xe000
	s_nop 0
	global_load_lds_dwordx4 v[188:189], off
	s_waitcnt lgkmcnt(8)
	s_barrier
	s_waitcnt lgkmcnt(0)
	v_cndmask_b32_e32 v188, v148, v140, vcc
	s_setprio 1
	s_waitcnt lgkmcnt(0)
	v_mfma_f32_16x16x128_f8f6f4 v[124:127], v[158:165], v[180:187], v[124:127]
	v_mfma_f32_16x16x128_f8f6f4 v[120:123], v[172:179], v[180:187], v[120:123]
	v_mfma_f32_16x16x128_f8f6f4 v[112:115], v[158:165], v[196:203], v[112:115]
	v_mfma_f32_16x16x128_f8f6f4 v[104:107], v[172:179], v[196:203], v[104:107]
	v_mfma_f32_16x16x128_f8f6f4 v[96:99], v[158:165], v[204:211], v[96:99]
	v_mfma_f32_16x16x128_f8f6f4 v[88:91], v[172:179], v[204:211], v[88:91]
	v_mfma_f32_16x16x128_f8f6f4 v[80:83], v[158:165], v[212:219], v[80:83]
	v_mfma_f32_16x16x128_f8f6f4 v[72:75], v[172:179], v[212:219], v[72:75]
	s_setprio 0
	s_barrier
	ds_read_b128 v[228:231], v167 offset:16384
	ds_read_b128 v[236:239], v167 offset:18432
	ds_read_b128 v[232:235], v168 offset:16384
	ds_read_b128 v[240:243], v168 offset:18432
	s_barrier
	s_waitcnt lgkmcnt(0)
	s_setprio 1
	s_waitcnt lgkmcnt(0)
	v_mfma_f32_16x16x128_f8f6f4 v[116:119], v[228:235], v[180:187], v[116:119]
	v_mfma_f32_16x16x128_f8f6f4 v[108:111], v[236:243], v[180:187], v[108:111]
	v_mfma_f32_16x16x128_f8f6f4 v[100:103], v[228:235], v[196:203], v[100:103]
	v_mfma_f32_16x16x128_f8f6f4 v[92:95], v[236:243], v[196:203], v[92:95]
	v_mfma_f32_16x16x128_f8f6f4 v[84:87], v[228:235], v[204:211], v[84:87]
	v_mfma_f32_16x16x128_f8f6f4 v[76:79], v[236:243], v[204:211], v[76:79]
	v_mfma_f32_16x16x128_f8f6f4 v[68:71], v[228:235], v[212:219], v[68:71]
	v_mfma_f32_16x16x128_f8f6f4 v[64:67], v[236:243], v[212:219], v[64:67]
	s_setprio 0
	s_barrier
	s_mov_b32 m0, s46
	ds_read_b128 v[196:199], v129 offset:16384
	ds_read_b128 v[204:207], v129 offset:18432
	ds_read_b128 v[200:203], v131 offset:16384
	ds_read_b128 v[208:211], v131 offset:18432
	ds_read_b128 v[212:215], v129 offset:20480
	ds_read_b128 v[220:223], v129 offset:22528
	ds_read_b128 v[216:219], v131 offset:20480
	ds_read_b128 v[224:227], v131 offset:22528
	global_load_lds_dwordx4 v136, s[38:39]
	s_mov_b32 m0, s49
	v_mov_b32_e32 v189, v137
	global_load_lds_dwordx4 v188, s[38:39]
	s_waitcnt lgkmcnt(8)
	s_barrier
	s_waitcnt lgkmcnt(0)
	v_lshl_add_u64 v[246:247], s[38:39], 0, v[136:137]
	v_lshl_add_u64 v[244:245], s[38:39], 0, v[188:189]
	s_setprio 1
	s_waitcnt lgkmcnt(0)
	v_mfma_f32_16x16x128_f8f6f4 v[60:63], v[158:165], v[196:203], v[60:63]
	v_mfma_f32_16x16x128_f8f6f4 v[56:59], v[172:179], v[196:203], v[56:59]
	v_mfma_f32_16x16x128_f8f6f4 v[48:51], v[158:165], v[204:211], v[48:51]
	v_mfma_f32_16x16x128_f8f6f4 v[40:43], v[172:179], v[204:211], v[40:43]
	v_mfma_f32_16x16x128_f8f6f4 v[32:35], v[158:165], v[212:219], v[32:35]
	v_mfma_f32_16x16x128_f8f6f4 v[24:27], v[172:179], v[212:219], v[24:27]
	v_mfma_f32_16x16x128_f8f6f4 v[16:19], v[158:165], v[220:227], v[16:19]
	v_mfma_f32_16x16x128_f8f6f4 v[8:11], v[172:179], v[220:227], v[8:11]
	s_setprio 0
	s_barrier
	s_mov_b32 m0, s47
	v_lshl_add_u64 v[158:159], s[36:37], 0, v[134:135]
	global_load_lds_dwordx4 v[158:159], off
	v_lshl_add_u64 v[160:161], s[36:37], 0, v[132:133]
	s_mov_b32 m0, s48
	s_nop 0
	global_load_lds_dwordx4 v[160:161], off
	s_waitcnt vmcnt(4)
	s_waitcnt lgkmcnt(0)
	s_barrier
	s_setprio 1
	s_waitcnt lgkmcnt(0)
	v_mfma_f32_16x16x128_f8f6f4 v[52:55], v[228:235], v[196:203], v[52:55]
	v_mfma_f32_16x16x128_f8f6f4 v[44:47], v[236:243], v[196:203], v[44:47]
	v_mfma_f32_16x16x128_f8f6f4 v[36:39], v[228:235], v[204:211], v[36:39]
	v_mfma_f32_16x16x128_f8f6f4 v[28:31], v[236:243], v[204:211], v[28:31]
	v_mfma_f32_16x16x128_f8f6f4 v[20:23], v[228:235], v[212:219], v[20:23]
	v_mfma_f32_16x16x128_f8f6f4 v[12:15], v[236:243], v[212:219], v[12:15]
	v_mfma_f32_16x16x128_f8f6f4 v[4:7], v[228:235], v[220:227], v[4:7]
	v_mfma_f32_16x16x128_f8f6f4 v[0:3], v[236:243], v[220:227], v[0:3]
	s_setprio 0
	s_barrier
	ds_read_b128 v[172:175], v167 offset:32768
	ds_read_b128 v[180:183], v167 offset:34816
	ds_read_b128 v[176:179], v168 offset:32768
	ds_read_b128 v[184:187], v168 offset:34816
	s_mov_b32 m0, s52
	ds_read_b128 v[196:199], v129 offset:32768
	ds_read_b128 v[204:207], v129 offset:34816
	ds_read_b128 v[200:203], v131 offset:32768
	ds_read_b128 v[208:211], v131 offset:34816
	ds_read_b128 v[212:215], v129 offset:36864
	ds_read_b128 v[220:223], v129 offset:38912
	ds_read_b128 v[216:219], v131 offset:36864
	ds_read_b128 v[224:227], v131 offset:38912
	v_cndmask_b32_e32 v136, v152, v144, vcc
	global_load_lds_dwordx4 v139, s[38:39]
	s_mov_b32 m0, s53
	s_nop 0
	global_load_lds_dwordx4 v136, s[38:39]
	s_add_u32 s38, s36, 0x1800
	s_addc_u32 s39, s37, 0
	v_lshl_add_u64 v[188:189], s[38:39], 0, v[134:135]
	s_mov_b32 m0, s50
	s_nop 0
	global_load_lds_dwordx4 v[188:189], off
	v_lshl_add_u64 v[188:189], s[38:39], 0, v[132:133]
	s_mov_b32 m0, s51
	s_nop 0
	global_load_lds_dwordx4 v[188:189], off
	s_waitcnt lgkmcnt(8)
	s_barrier
	s_waitcnt lgkmcnt(0)
	s_setprio 1
	s_waitcnt lgkmcnt(0)
	v_mfma_f32_16x16x128_f8f6f4 v[124:127], v[172:179], v[196:203], v[124:127]
	v_mfma_f32_16x16x128_f8f6f4 v[120:123], v[180:187], v[196:203], v[120:123]
	v_mfma_f32_16x16x128_f8f6f4 v[112:115], v[172:179], v[204:211], v[112:115]
	v_mfma_f32_16x16x128_f8f6f4 v[104:107], v[180:187], v[204:211], v[104:107]
	v_mfma_f32_16x16x128_f8f6f4 v[96:99], v[172:179], v[212:219], v[96:99]
	v_mfma_f32_16x16x128_f8f6f4 v[88:91], v[180:187], v[212:219], v[88:91]
	v_mfma_f32_16x16x128_f8f6f4 v[80:83], v[172:179], v[220:227], v[80:83]
	v_mfma_f32_16x16x128_f8f6f4 v[72:75], v[180:187], v[220:227], v[72:75]
	s_setprio 0
	s_barrier
	ds_read_b128 v[228:231], v167 offset:49152
	ds_read_b128 v[236:239], v167 offset:51200
	ds_read_b128 v[232:235], v168 offset:49152
	ds_read_b128 v[240:243], v168 offset:51200
	s_barrier
	s_waitcnt lgkmcnt(0)
	s_setprio 1
	s_waitcnt lgkmcnt(0)
	v_mfma_f32_16x16x128_f8f6f4 v[116:119], v[228:235], v[196:203], v[116:119]
	v_mfma_f32_16x16x128_f8f6f4 v[108:111], v[236:243], v[196:203], v[108:111]
	v_mfma_f32_16x16x128_f8f6f4 v[100:103], v[228:235], v[204:211], v[100:103]
	v_mfma_f32_16x16x128_f8f6f4 v[92:95], v[236:243], v[204:211], v[92:95]
	v_mfma_f32_16x16x128_f8f6f4 v[84:87], v[228:235], v[212:219], v[84:87]
	v_mfma_f32_16x16x128_f8f6f4 v[76:79], v[236:243], v[212:219], v[76:79]
	v_mfma_f32_16x16x128_f8f6f4 v[68:71], v[228:235], v[220:227], v[68:71]
	v_mfma_f32_16x16x128_f8f6f4 v[64:67], v[236:243], v[220:227], v[64:67]
	s_setprio 0
	s_barrier
	s_mov_b32 m0, s56
	v_lshl_add_u64 v[246:247], v[246:247], 0, s[18:19]
	ds_read_b128 v[196:199], v129 offset:49152
	ds_read_b128 v[204:207], v129 offset:51200
	ds_read_b128 v[200:203], v131 offset:49152
	ds_read_b128 v[208:211], v131 offset:51200
	ds_read_b128 v[212:215], v129 offset:53248
	ds_read_b128 v[220:223], v129 offset:55296
	ds_read_b128 v[216:219], v131 offset:53248
	ds_read_b128 v[224:227], v131 offset:55296
	global_load_lds_dwordx4 v[246:247], off
	v_lshl_add_u64 v[244:245], v[244:245], 0, s[18:19]
	s_mov_b32 m0, s57
	s_nop 0
	global_load_lds_dwordx4 v[244:245], off
	s_waitcnt lgkmcnt(8)
	s_barrier
	s_waitcnt lgkmcnt(0)
	s_setprio 1
	s_waitcnt lgkmcnt(0)
	v_mfma_f32_16x16x128_f8f6f4 v[60:63], v[172:179], v[196:203], v[60:63]
	v_mfma_f32_16x16x128_f8f6f4 v[56:59], v[180:187], v[196:203], v[56:59]
	v_mfma_f32_16x16x128_f8f6f4 v[48:51], v[172:179], v[204:211], v[48:51]
	v_mfma_f32_16x16x128_f8f6f4 v[40:43], v[180:187], v[204:211], v[40:43]
	v_mfma_f32_16x16x128_f8f6f4 v[32:35], v[172:179], v[212:219], v[32:35]
	v_mfma_f32_16x16x128_f8f6f4 v[24:27], v[180:187], v[212:219], v[24:27]
	v_mfma_f32_16x16x128_f8f6f4 v[16:19], v[172:179], v[220:227], v[16:19]
	v_mfma_f32_16x16x128_f8f6f4 v[8:11], v[180:187], v[220:227], v[8:11]
	s_setprio 0
	s_barrier
	s_mov_b32 m0, s54
	v_lshl_add_u64 v[158:159], v[158:159], 0, s[18:19]
	global_load_lds_dwordx4 v[158:159], off
	v_lshl_add_u64 v[158:159], v[160:161], 0, s[18:19]
	s_mov_b32 m0, s55
	s_nop 0
	global_load_lds_dwordx4 v[158:159], off
	s_waitcnt vmcnt(4)
	s_waitcnt lgkmcnt(0)
	s_barrier
	s_setprio 1
	s_waitcnt lgkmcnt(0)
	v_mfma_f32_16x16x128_f8f6f4 v[52:55], v[228:235], v[196:203], v[52:55]
	v_mfma_f32_16x16x128_f8f6f4 v[44:47], v[236:243], v[196:203], v[44:47]
	v_mfma_f32_16x16x128_f8f6f4 v[36:39], v[228:235], v[204:211], v[36:39]
	v_mfma_f32_16x16x128_f8f6f4 v[28:31], v[236:243], v[204:211], v[28:31]
	v_mfma_f32_16x16x128_f8f6f4 v[20:23], v[228:235], v[212:219], v[20:23]
	v_mfma_f32_16x16x128_f8f6f4 v[12:15], v[236:243], v[212:219], v[12:15]
	v_mfma_f32_16x16x128_f8f6f4 v[4:7], v[228:235], v[220:227], v[4:7]
	v_mfma_f32_16x16x128_f8f6f4 v[0:3], v[236:243], v[220:227], v[0:3]
	s_setprio 0
	s_barrier
	s_add_u32 s36, s36, 0x1880
	s_addc_u32 s37, s37, 0
	s_mov_b32 m0, s58
	v_lshl_add_u64 v[158:159], s[36:37], 0, v[134:135]
	global_load_lds_dwordx4 v[158:159], off
	v_lshl_add_u64 v[158:159], s[36:37], 0, v[132:133]
	s_mov_b32 m0, s59
	s_add_i32 s69, s69, 2
	global_load_lds_dwordx4 v[158:159], off
	s_add_u32 s34, s34, 0x100
	s_addc_u32 s35, s35, 0
	s_cmp_gt_u32 s69, 3
	s_cbranch_scc0 .LBB0_313
	s_and_b64 vcc, exec, s[24:25]
	s_cbranch_vccz .LBB0_316
	s_barrier

.LBB0_756:
	s_add_u32 s38, s8, s36
	s_addc_u32 s39, s9, s37
	s_add_u32 s40, s38, 0x14000100
	ds_read_b128 v[144:147], v154
	ds_read_b128 v[168:171], v154 offset:2048
	ds_read_b128 v[148:151], v155
	ds_read_b128 v[172:175], v155 offset:2048
	s_addc_u32 s41, s39, 0
	s_add_u32 s68, s0, s36
	s_addc_u32 s69, s1, s37
	s_cmpk_eq_i32 s36, 0x700
	s_cselect_b64 vcc, -1, 0
	s_and_b64 s[38:39], vcc, exec
	v_cndmask_b32_e32 v132, v166, v162, vcc
	s_cselect_b32 s41, s11, s41
	s_cselect_b32 s40, s10, s40
	s_cselect_b32 s39, s31, s69
	s_cselect_b32 s38, s30, s68
	v_cndmask_b32_e32 v137, v136, v164, vcc
	s_mov_b32 m0, s66
	v_lshl_add_u64 v[192:193], v[142:143], 0, s[36:37]
	ds_read_b128 v[176:179], v152
	ds_read_b128 v[184:187], v152 offset:2048
	ds_read_b128 v[180:183], v153
	ds_read_b128 v[188:191], v153 offset:2048
	ds_read_b128 v[196:199], v152 offset:4096
	ds_read_b128 v[204:207], v152 offset:6144
	ds_read_b128 v[200:203], v153 offset:4096
	ds_read_b128 v[208:211], v153 offset:6144
	global_load_lds_dwordx4 v[192:193], off
	v_lshl_add_u64 v[192:193], v[140:141], 0, s[36:37]
	s_mov_b32 m0, s67
	s_nop 0
	global_load_lds_dwordx4 v[192:193], off
	s_waitcnt lgkmcnt(8)
	s_barrier
	s_waitcnt lgkmcnt(0)
	v_cndmask_b32_e32 v192, v134, v163, vcc
	s_setprio 1
	s_waitcnt lgkmcnt(0)
	v_mfma_f32_16x16x128_f8f6f4 v[124:127], v[144:151], v[176:183], v[124:127]
	v_mfma_f32_16x16x128_f8f6f4 v[120:123], v[168:175], v[176:183], v[120:123]
	v_mfma_f32_16x16x128_f8f6f4 v[108:111], v[144:151], v[184:191], v[108:111]
	v_mfma_f32_16x16x128_f8f6f4 v[104:107], v[168:175], v[184:191], v[104:107]
	v_mfma_f32_16x16x128_f8f6f4 v[92:95], v[144:151], v[196:203], v[92:95]
	v_mfma_f32_16x16x128_f8f6f4 v[88:91], v[168:175], v[196:203], v[88:91]
	v_mfma_f32_16x16x128_f8f6f4 v[76:79], v[144:151], v[204:211], v[76:79]
	v_mfma_f32_16x16x128_f8f6f4 v[72:75], v[168:175], v[204:211], v[72:75]
	s_setprio 0
	s_barrier
	ds_read_b128 v[234:237], v154 offset:16384
	ds_read_b128 v[242:245], v154 offset:18432
	ds_read_b128 v[238:241], v155 offset:16384
	ds_read_b128 v[246:249], v155 offset:18432
	s_barrier
	s_waitcnt lgkmcnt(0)
	s_setprio 1
	s_waitcnt lgkmcnt(0)
	v_mfma_f32_16x16x128_f8f6f4 v[116:119], v[234:241], v[176:183], v[116:119]
	v_mfma_f32_16x16x128_f8f6f4 v[112:115], v[242:249], v[176:183], v[112:115]
	v_mfma_f32_16x16x128_f8f6f4 v[100:103], v[234:241], v[184:191], v[100:103]
	v_mfma_f32_16x16x128_f8f6f4 v[96:99], v[242:249], v[184:191], v[96:99]
	v_mfma_f32_16x16x128_f8f6f4 v[84:87], v[234:241], v[196:203], v[84:87]
	v_mfma_f32_16x16x128_f8f6f4 v[80:83], v[242:249], v[196:203], v[80:83]
	v_mfma_f32_16x16x128_f8f6f4 v[68:71], v[234:241], v[204:211], v[68:71]
	v_mfma_f32_16x16x128_f8f6f4 v[64:67], v[242:249], v[204:211], v[64:67]
	s_setprio 0
	s_barrier
	s_mov_b32 m0, s35
	ds_read_b128 v[184:187], v152 offset:16384
	ds_read_b128 v[196:199], v152 offset:18432
	ds_read_b128 v[188:191], v153 offset:16384
	ds_read_b128 v[200:203], v153 offset:18432
	ds_read_b128 v[204:207], v152 offset:20480
	ds_read_b128 v[212:215], v152 offset:22528
	ds_read_b128 v[208:211], v153 offset:20480
	ds_read_b128 v[216:219], v153 offset:22528
	global_load_lds_dwordx4 v132, s[40:41]
	s_mov_b32 m0, s45
	v_mov_b32_e32 v193, v133
	global_load_lds_dwordx4 v192, s[40:41]
	s_waitcnt lgkmcnt(8)
	s_barrier
	s_waitcnt lgkmcnt(0)
	v_lshl_add_u64 v[252:253], s[40:41], 0, v[132:133]
	v_lshl_add_u64 v[250:251], s[40:41], 0, v[192:193]
	s_setprio 1
	s_waitcnt lgkmcnt(0)
	v_mfma_f32_16x16x128_f8f6f4 v[60:63], v[144:151], v[184:191], v[60:63]
	v_mfma_f32_16x16x128_f8f6f4 v[56:59], v[168:175], v[184:191], v[56:59]
	v_mfma_f32_16x16x128_f8f6f4 v[44:47], v[144:151], v[196:203], v[44:47]
	v_mfma_f32_16x16x128_f8f6f4 v[40:43], v[168:175], v[196:203], v[40:43]
	v_mfma_f32_16x16x128_f8f6f4 v[28:31], v[144:151], v[204:211], v[28:31]
	v_mfma_f32_16x16x128_f8f6f4 v[24:27], v[168:175], v[204:211], v[24:27]
	v_mfma_f32_16x16x128_f8f6f4 v[12:15], v[144:151], v[212:219], v[12:15]
	v_mfma_f32_16x16x128_f8f6f4 v[8:11], v[168:175], v[212:219], v[8:11]
	s_setprio 0
	s_barrier
	s_mov_b32 m0, s43
	v_lshl_add_u64 v[144:145], s[38:39], 0, v[130:131]
	global_load_lds_dwordx4 v[144:145], off
	v_lshl_add_u64 v[146:147], s[38:39], 0, v[128:129]
	s_mov_b32 m0, s44
	s_nop 0
	global_load_lds_dwordx4 v[146:147], off
	s_waitcnt vmcnt(4)
	s_waitcnt lgkmcnt(0)
	s_barrier
	s_setprio 1
	s_waitcnt lgkmcnt(0)
	v_mfma_f32_16x16x128_f8f6f4 v[52:55], v[234:241], v[184:191], v[52:55]
	v_mfma_f32_16x16x128_f8f6f4 v[48:51], v[242:249], v[184:191], v[48:51]
	v_mfma_f32_16x16x128_f8f6f4 v[36:39], v[234:241], v[196:203], v[36:39]
	v_mfma_f32_16x16x128_f8f6f4 v[32:35], v[242:249], v[196:203], v[32:35]
	v_mfma_f32_16x16x128_f8f6f4 v[20:23], v[234:241], v[204:211], v[20:23]
	v_mfma_f32_16x16x128_f8f6f4 v[16:19], v[242:249], v[204:211], v[16:19]
	v_mfma_f32_16x16x128_f8f6f4 v[4:7], v[234:241], v[212:219], v[4:7]
	v_mfma_f32_16x16x128_f8f6f4 v[0:3], v[242:249], v[212:219], v[0:3]
	s_setprio 0
	s_barrier
	ds_read_b128 v[168:171], v154 offset:32768
	ds_read_b128 v[176:179], v154 offset:34816
	ds_read_b128 v[172:175], v155 offset:32768
	ds_read_b128 v[180:183], v155 offset:34816
	s_mov_b32 m0, s48
	ds_read_b128 v[184:187], v152 offset:32768
	ds_read_b128 v[196:199], v152 offset:34816
	ds_read_b128 v[188:191], v153 offset:32768
	ds_read_b128 v[200:203], v153 offset:34816
	ds_read_b128 v[204:207], v152 offset:36864
	ds_read_b128 v[212:215], v152 offset:38912
	ds_read_b128 v[208:211], v153 offset:36864
	ds_read_b128 v[216:219], v153 offset:38912
	v_cndmask_b32_e32 v132, v138, v165, vcc
	global_load_lds_dwordx4 v137, s[40:41]
	s_mov_b32 m0, s49
	s_nop 0
	global_load_lds_dwordx4 v132, s[40:41]
	s_add_u32 s40, s38, 0x4000
	s_addc_u32 s41, s39, 0
	v_lshl_add_u64 v[192:193], s[40:41], 0, v[130:131]
	s_mov_b32 m0, s46
	s_nop 0
	global_load_lds_dwordx4 v[192:193], off
	v_lshl_add_u64 v[192:193], s[40:41], 0, v[128:129]
	s_mov_b32 m0, s47
	s_nop 0
	global_load_lds_dwordx4 v[192:193], off
	s_waitcnt lgkmcnt(8)
	s_barrier
	s_waitcnt lgkmcnt(0)
	s_setprio 1
	s_waitcnt lgkmcnt(0)
	v_mfma_f32_16x16x128_f8f6f4 v[124:127], v[168:175], v[184:191], v[124:127]
	v_mfma_f32_16x16x128_f8f6f4 v[120:123], v[176:183], v[184:191], v[120:123]
	v_mfma_f32_16x16x128_f8f6f4 v[108:111], v[168:175], v[196:203], v[108:111]
	v_mfma_f32_16x16x128_f8f6f4 v[104:107], v[176:183], v[196:203], v[104:107]
	v_mfma_f32_16x16x128_f8f6f4 v[92:95], v[168:175], v[204:211], v[92:95]
	v_mfma_f32_16x16x128_f8f6f4 v[88:91], v[176:183], v[204:211], v[88:91]
	v_mfma_f32_16x16x128_f8f6f4 v[76:79], v[168:175], v[212:219], v[76:79]
	v_mfma_f32_16x16x128_f8f6f4 v[72:75], v[176:183], v[212:219], v[72:75]
	s_setprio 0
	s_barrier
	ds_read_b128 v[234:237], v154 offset:49152
	ds_read_b128 v[242:245], v154 offset:51200
	ds_read_b128 v[238:241], v155 offset:49152
	ds_read_b128 v[246:249], v155 offset:51200
	s_barrier
	s_waitcnt lgkmcnt(0)
	s_setprio 1
	s_waitcnt lgkmcnt(0)
	v_mfma_f32_16x16x128_f8f6f4 v[116:119], v[234:241], v[184:191], v[116:119]
	v_mfma_f32_16x16x128_f8f6f4 v[112:115], v[242:249], v[184:191], v[112:115]
	v_mfma_f32_16x16x128_f8f6f4 v[100:103], v[234:241], v[196:203], v[100:103]
	v_mfma_f32_16x16x128_f8f6f4 v[96:99], v[242:249], v[196:203], v[96:99]
	v_mfma_f32_16x16x128_f8f6f4 v[84:87], v[234:241], v[204:211], v[84:87]
	v_mfma_f32_16x16x128_f8f6f4 v[80:83], v[242:249], v[204:211], v[80:83]
	v_mfma_f32_16x16x128_f8f6f4 v[68:71], v[234:241], v[212:219], v[68:71]
	v_mfma_f32_16x16x128_f8f6f4 v[64:67], v[242:249], v[212:219], v[64:67]
	s_setprio 0
	s_barrier
	s_mov_b32 m0, s60
	v_lshl_add_u64 v[252:253], v[252:253], 0, s[16:17]
	ds_read_b128 v[184:187], v152 offset:49152
	ds_read_b128 v[196:199], v152 offset:51200
	ds_read_b128 v[188:191], v153 offset:49152
	ds_read_b128 v[200:203], v153 offset:51200
	ds_read_b128 v[204:207], v152 offset:53248
	ds_read_b128 v[212:215], v152 offset:55296
	ds_read_b128 v[208:211], v153 offset:53248
	ds_read_b128 v[216:219], v153 offset:55296
	global_load_lds_dwordx4 v[252:253], off
	v_lshl_add_u64 v[250:251], v[250:251], 0, s[16:17]
	s_mov_b32 m0, s61
	s_nop 0
	global_load_lds_dwordx4 v[250:251], off
	s_waitcnt lgkmcnt(8)
	s_barrier
	s_waitcnt lgkmcnt(0)
	s_setprio 1
	s_waitcnt lgkmcnt(0)
	v_mfma_f32_16x16x128_f8f6f4 v[60:63], v[168:175], v[184:191], v[60:63]
	v_mfma_f32_16x16x128_f8f6f4 v[56:59], v[176:183], v[184:191], v[56:59]
	v_mfma_f32_16x16x128_f8f6f4 v[44:47], v[168:175], v[196:203], v[44:47]
	v_mfma_f32_16x16x128_f8f6f4 v[40:43], v[176:183], v[196:203], v[40:43]
	v_mfma_f32_16x16x128_f8f6f4 v[28:31], v[168:175], v[204:211], v[28:31]
	v_mfma_f32_16x16x128_f8f6f4 v[24:27], v[176:183], v[204:211], v[24:27]
	v_mfma_f32_16x16x128_f8f6f4 v[12:15], v[168:175], v[212:219], v[12:15]
	v_mfma_f32_16x16x128_f8f6f4 v[8:11], v[176:183], v[212:219], v[8:11]
	s_setprio 0
	s_barrier
	s_mov_b32 m0, s58
	v_lshl_add_u64 v[144:145], v[144:145], 0, s[16:17]
	global_load_lds_dwordx4 v[144:145], off
	v_lshl_add_u64 v[144:145], v[146:147], 0, s[16:17]
	s_mov_b32 m0, s59
	s_nop 0
	global_load_lds_dwordx4 v[144:145], off
	s_waitcnt vmcnt(4)
	s_waitcnt lgkmcnt(0)
	s_barrier
	s_setprio 1
	s_waitcnt lgkmcnt(0)
	v_mfma_f32_16x16x128_f8f6f4 v[52:55], v[234:241], v[184:191], v[52:55]
	v_mfma_f32_16x16x128_f8f6f4 v[48:51], v[242:249], v[184:191], v[48:51]
	v_mfma_f32_16x16x128_f8f6f4 v[36:39], v[234:241], v[196:203], v[36:39]
	v_mfma_f32_16x16x128_f8f6f4 v[32:35], v[242:249], v[196:203], v[32:35]
	v_mfma_f32_16x16x128_f8f6f4 v[20:23], v[234:241], v[204:211], v[20:23]
	v_mfma_f32_16x16x128_f8f6f4 v[16:19], v[242:249], v[204:211], v[16:19]
	v_mfma_f32_16x16x128_f8f6f4 v[4:7], v[234:241], v[212:219], v[4:7]
	v_mfma_f32_16x16x128_f8f6f4 v[0:3], v[242:249], v[212:219], v[0:3]
	s_setprio 0
	s_barrier
	s_add_u32 s38, s38, 0x4080
	s_addc_u32 s39, s39, 0
	s_mov_b32 m0, s62
	v_lshl_add_u64 v[144:145], s[38:39], 0, v[130:131]
	global_load_lds_dwordx4 v[144:145], off
	v_lshl_add_u64 v[144:145], s[38:39], 0, v[128:129]
	s_mov_b32 m0, s63
	s_add_i32 s57, s57, 2
	global_load_lds_dwordx4 v[144:145], off
	s_add_u32 s36, s36, 0x100
	s_addc_u32 s37, s37, 0
	s_cmp_gt_u32 s57, 13
	s_cbranch_scc0 .LBB0_756
	s_and_b64 vcc, exec, s[20:21]
	s_cbranch_vccz .LBB0_759
	s_barrier

.LBB0_1503:
	s_add_u32 s36, s8, s34
	s_addc_u32 s37, s9, s35
	s_add_u32 s38, s36, 0x6ea00100
	ds_read_b128 v[144:147], v168
	ds_read_b128 v[152:155], v168 offset:2048
	ds_read_b128 v[148:151], v169
	ds_read_b128 v[156:159], v169 offset:2048
	s_addc_u32 s39, s37, 0
	s_add_u32 s60, s56, s34
	s_addc_u32 s61, s57, s35
	s_cmpk_eq_i32 s34, 0x700
	s_cselect_b64 vcc, -1, 0
	s_and_b64 s[36:37], vcc, exec
	v_cndmask_b32_e32 v132, v135, v179, vcc
	s_cselect_b32 s39, s11, s39
	s_cselect_b32 s38, s10, s38
	s_cselect_b32 s37, s31, s61
	s_cselect_b32 s36, s30, s60
	v_cndmask_b32_e32 v137, v136, v181, vcc
	v_lshl_add_u64 v[160:161], v[142:143], 0, s[34:35]
	s_add_i32 m0, s27, 0xc000
	ds_read_b128 v[184:187], v166
	ds_read_b128 v[196:199], v166 offset:2048
	ds_read_b128 v[188:191], v167
	ds_read_b128 v[200:203], v167 offset:2048
	ds_read_b128 v[204:207], v166 offset:4096
	ds_read_b128 v[212:215], v166 offset:6144
	ds_read_b128 v[208:211], v167 offset:4096
	ds_read_b128 v[216:219], v167 offset:6144
	global_load_lds_dwordx4 v[160:161], off
	v_lshl_add_u64 v[160:161], v[140:141], 0, s[34:35]
	s_add_i32 m0, s27, 0xe000
	s_nop 0
	global_load_lds_dwordx4 v[160:161], off
	s_waitcnt lgkmcnt(8)
	s_barrier
	s_waitcnt lgkmcnt(0)
	v_cndmask_b32_e32 v160, v134, v180, vcc
	s_setprio 1
	s_waitcnt lgkmcnt(0)
	v_mfma_f32_16x16x128_f8f6f4 v[124:127], v[144:151], v[184:191], v[124:127]
	v_mfma_f32_16x16x128_f8f6f4 v[120:123], v[152:159], v[184:191], v[120:123]
	v_mfma_f32_16x16x128_f8f6f4 v[112:115], v[144:151], v[196:203], v[112:115]
	v_mfma_f32_16x16x128_f8f6f4 v[104:107], v[152:159], v[196:203], v[104:107]
	v_mfma_f32_16x16x128_f8f6f4 v[96:99], v[144:151], v[204:211], v[96:99]
	v_mfma_f32_16x16x128_f8f6f4 v[88:91], v[152:159], v[204:211], v[88:91]
	v_mfma_f32_16x16x128_f8f6f4 v[80:83], v[144:151], v[212:219], v[80:83]
	v_mfma_f32_16x16x128_f8f6f4 v[72:75], v[152:159], v[212:219], v[72:75]
	s_setprio 0
	s_barrier
	ds_read_b128 v[228:231], v168 offset:16384
	ds_read_b128 v[236:239], v168 offset:18432
	ds_read_b128 v[232:235], v169 offset:16384
	ds_read_b128 v[240:243], v169 offset:18432
	s_barrier
	s_waitcnt lgkmcnt(0)
	s_setprio 1
	s_waitcnt lgkmcnt(0)
	v_mfma_f32_16x16x128_f8f6f4 v[116:119], v[228:235], v[184:191], v[116:119]
	v_mfma_f32_16x16x128_f8f6f4 v[108:111], v[236:243], v[184:191], v[108:111]
	v_mfma_f32_16x16x128_f8f6f4 v[100:103], v[228:235], v[196:203], v[100:103]
	v_mfma_f32_16x16x128_f8f6f4 v[92:95], v[236:243], v[196:203], v[92:95]
	v_mfma_f32_16x16x128_f8f6f4 v[84:87], v[228:235], v[204:211], v[84:87]
	v_mfma_f32_16x16x128_f8f6f4 v[76:79], v[236:243], v[204:211], v[76:79]
	v_mfma_f32_16x16x128_f8f6f4 v[68:71], v[228:235], v[212:219], v[68:71]
	v_mfma_f32_16x16x128_f8f6f4 v[64:67], v[236:243], v[212:219], v[64:67]
	s_setprio 0
	s_barrier
	s_mov_b32 m0, s27
	ds_read_b128 v[196:199], v166 offset:16384
	ds_read_b128 v[204:207], v166 offset:18432
	ds_read_b128 v[200:203], v167 offset:16384
	ds_read_b128 v[208:211], v167 offset:18432
	ds_read_b128 v[212:215], v166 offset:20480
	ds_read_b128 v[220:223], v166 offset:22528
	ds_read_b128 v[216:219], v167 offset:20480
	ds_read_b128 v[224:227], v167 offset:22528
	global_load_lds_dwordx4 v132, s[38:39]
	s_mov_b32 m0, s41
	v_mov_b32_e32 v161, v133
	global_load_lds_dwordx4 v160, s[38:39]
	s_waitcnt lgkmcnt(8)
	s_barrier
	s_waitcnt lgkmcnt(0)
	v_lshl_add_u64 v[246:247], s[38:39], 0, v[132:133]
	v_lshl_add_u64 v[244:245], s[38:39], 0, v[160:161]
	s_setprio 1
	s_waitcnt lgkmcnt(0)
	v_mfma_f32_16x16x128_f8f6f4 v[60:63], v[144:151], v[196:203], v[60:63]
	v_mfma_f32_16x16x128_f8f6f4 v[56:59], v[152:159], v[196:203], v[56:59]
	v_mfma_f32_16x16x128_f8f6f4 v[48:51], v[144:151], v[204:211], v[48:51]
	v_mfma_f32_16x16x128_f8f6f4 v[40:43], v[152:159], v[204:211], v[40:43]
	v_mfma_f32_16x16x128_f8f6f4 v[32:35], v[144:151], v[212:219], v[32:35]
	v_mfma_f32_16x16x128_f8f6f4 v[24:27], v[152:159], v[212:219], v[24:27]
	v_mfma_f32_16x16x128_f8f6f4 v[16:19], v[144:151], v[220:227], v[16:19]
	v_mfma_f32_16x16x128_f8f6f4 v[8:11], v[152:159], v[220:227], v[8:11]
	s_setprio 0
	s_barrier
	s_mov_b32 m0, s33
	v_lshl_add_u64 v[144:145], s[36:37], 0, v[128:129]
	global_load_lds_dwordx4 v[144:145], off
	v_lshl_add_u64 v[146:147], s[36:37], 0, v[130:131]
	s_mov_b32 m0, s40
	s_nop 0
	global_load_lds_dwordx4 v[146:147], off
	s_waitcnt vmcnt(4)
	s_waitcnt lgkmcnt(0)
	s_barrier
	s_setprio 1
	s_waitcnt lgkmcnt(0)
	v_mfma_f32_16x16x128_f8f6f4 v[52:55], v[228:235], v[196:203], v[52:55]
	v_mfma_f32_16x16x128_f8f6f4 v[44:47], v[236:243], v[196:203], v[44:47]
	v_mfma_f32_16x16x128_f8f6f4 v[36:39], v[228:235], v[204:211], v[36:39]
	v_mfma_f32_16x16x128_f8f6f4 v[28:31], v[236:243], v[204:211], v[28:31]
	v_mfma_f32_16x16x128_f8f6f4 v[20:23], v[228:235], v[212:219], v[20:23]
	v_mfma_f32_16x16x128_f8f6f4 v[12:15], v[236:243], v[212:219], v[12:15]
	v_mfma_f32_16x16x128_f8f6f4 v[4:7], v[228:235], v[220:227], v[4:7]
	v_mfma_f32_16x16x128_f8f6f4 v[0:3], v[236:243], v[220:227], v[0:3]
	s_setprio 0
	s_barrier
	ds_read_b128 v[152:155], v168 offset:32768
	ds_read_b128 v[184:187], v168 offset:34816
	ds_read_b128 v[156:159], v169 offset:32768
	ds_read_b128 v[188:191], v169 offset:34816
	s_mov_b32 m0, s44
	ds_read_b128 v[196:199], v166 offset:32768
	ds_read_b128 v[204:207], v166 offset:34816
	ds_read_b128 v[200:203], v167 offset:32768
	ds_read_b128 v[208:211], v167 offset:34816
	ds_read_b128 v[212:215], v166 offset:36864
	ds_read_b128 v[220:223], v166 offset:38912
	ds_read_b128 v[216:219], v167 offset:36864
	ds_read_b128 v[224:227], v167 offset:38912
	v_cndmask_b32_e32 v132, v138, v182, vcc
	global_load_lds_dwordx4 v137, s[38:39]
	s_mov_b32 m0, s45
	s_nop 0
	global_load_lds_dwordx4 v132, s[38:39]
	s_add_u32 s38, s36, 0x40000
	s_addc_u32 s39, s37, 0
	v_lshl_add_u64 v[160:161], s[38:39], 0, v[128:129]
	s_mov_b32 m0, s42
	s_nop 0
	global_load_lds_dwordx4 v[160:161], off
	v_lshl_add_u64 v[160:161], s[38:39], 0, v[130:131]
	s_mov_b32 m0, s43
	s_nop 0
	global_load_lds_dwordx4 v[160:161], off
	s_waitcnt lgkmcnt(8)
	s_barrier
	s_waitcnt lgkmcnt(0)
	s_setprio 1
	s_waitcnt lgkmcnt(0)
	v_mfma_f32_16x16x128_f8f6f4 v[124:127], v[152:159], v[196:203], v[124:127]
	v_mfma_f32_16x16x128_f8f6f4 v[120:123], v[184:191], v[196:203], v[120:123]
	v_mfma_f32_16x16x128_f8f6f4 v[112:115], v[152:159], v[204:211], v[112:115]
	v_mfma_f32_16x16x128_f8f6f4 v[104:107], v[184:191], v[204:211], v[104:107]
	v_mfma_f32_16x16x128_f8f6f4 v[96:99], v[152:159], v[212:219], v[96:99]
	v_mfma_f32_16x16x128_f8f6f4 v[88:91], v[184:191], v[212:219], v[88:91]
	v_mfma_f32_16x16x128_f8f6f4 v[80:83], v[152:159], v[220:227], v[80:83]
	v_mfma_f32_16x16x128_f8f6f4 v[72:75], v[184:191], v[220:227], v[72:75]
	s_setprio 0
	s_barrier
	ds_read_b128 v[228:231], v168 offset:49152
	ds_read_b128 v[236:239], v168 offset:51200
	ds_read_b128 v[232:235], v169 offset:49152
	ds_read_b128 v[240:243], v169 offset:51200
	s_barrier
	s_waitcnt lgkmcnt(0)
	s_setprio 1
	s_waitcnt lgkmcnt(0)
	v_mfma_f32_16x16x128_f8f6f4 v[116:119], v[228:235], v[196:203], v[116:119]
	v_mfma_f32_16x16x128_f8f6f4 v[108:111], v[236:243], v[196:203], v[108:111]
	v_mfma_f32_16x16x128_f8f6f4 v[100:103], v[228:235], v[204:211], v[100:103]
	v_mfma_f32_16x16x128_f8f6f4 v[92:95], v[236:243], v[204:211], v[92:95]
	v_mfma_f32_16x16x128_f8f6f4 v[84:87], v[228:235], v[212:219], v[84:87]
	v_mfma_f32_16x16x128_f8f6f4 v[76:79], v[236:243], v[212:219], v[76:79]
	v_mfma_f32_16x16x128_f8f6f4 v[68:71], v[228:235], v[220:227], v[68:71]
	v_mfma_f32_16x16x128_f8f6f4 v[64:67], v[236:243], v[220:227], v[64:67]
	s_setprio 0
	s_barrier
	s_mov_b32 m0, s50
	v_lshl_add_u64 v[246:247], v[246:247], 0, s[16:17]
	ds_read_b128 v[196:199], v166 offset:49152
	ds_read_b128 v[204:207], v166 offset:51200
	ds_read_b128 v[200:203], v167 offset:49152
	ds_read_b128 v[208:211], v167 offset:51200
	ds_read_b128 v[212:215], v166 offset:53248
	ds_read_b128 v[220:223], v166 offset:55296
	ds_read_b128 v[216:219], v167 offset:53248
	ds_read_b128 v[224:227], v167 offset:55296
	global_load_lds_dwordx4 v[246:247], off
	v_lshl_add_u64 v[244:245], v[244:245], 0, s[16:17]
	s_mov_b32 m0, s51
	s_nop 0
	global_load_lds_dwordx4 v[244:245], off
	s_waitcnt lgkmcnt(8)
	s_barrier
	s_waitcnt lgkmcnt(0)
	s_setprio 1
	s_waitcnt lgkmcnt(0)
	v_mfma_f32_16x16x128_f8f6f4 v[60:63], v[152:159], v[196:203], v[60:63]
	v_mfma_f32_16x16x128_f8f6f4 v[56:59], v[184:191], v[196:203], v[56:59]
	v_mfma_f32_16x16x128_f8f6f4 v[48:51], v[152:159], v[204:211], v[48:51]
	v_mfma_f32_16x16x128_f8f6f4 v[40:43], v[184:191], v[204:211], v[40:43]
	v_mfma_f32_16x16x128_f8f6f4 v[32:35], v[152:159], v[212:219], v[32:35]
	v_mfma_f32_16x16x128_f8f6f4 v[24:27], v[184:191], v[212:219], v[24:27]
	v_mfma_f32_16x16x128_f8f6f4 v[16:19], v[152:159], v[220:227], v[16:19]
	v_mfma_f32_16x16x128_f8f6f4 v[8:11], v[184:191], v[220:227], v[8:11]
	s_setprio 0
	s_barrier
	s_mov_b32 m0, s48
	v_lshl_add_u64 v[144:145], v[144:145], 0, s[16:17]
	global_load_lds_dwordx4 v[144:145], off
	v_lshl_add_u64 v[144:145], v[146:147], 0, s[16:17]
	s_mov_b32 m0, s49
	s_nop 0
	global_load_lds_dwordx4 v[144:145], off
	s_waitcnt vmcnt(4)
	s_waitcnt lgkmcnt(0)
	s_barrier
	s_setprio 1
	s_waitcnt lgkmcnt(0)
	v_mfma_f32_16x16x128_f8f6f4 v[52:55], v[228:235], v[196:203], v[52:55]
	v_mfma_f32_16x16x128_f8f6f4 v[44:47], v[236:243], v[196:203], v[44:47]
	v_mfma_f32_16x16x128_f8f6f4 v[36:39], v[228:235], v[204:211], v[36:39]
	v_mfma_f32_16x16x128_f8f6f4 v[28:31], v[236:243], v[204:211], v[28:31]
	v_mfma_f32_16x16x128_f8f6f4 v[20:23], v[228:235], v[212:219], v[20:23]
	v_mfma_f32_16x16x128_f8f6f4 v[12:15], v[236:243], v[212:219], v[12:15]
	v_mfma_f32_16x16x128_f8f6f4 v[4:7], v[228:235], v[220:227], v[4:7]
	v_mfma_f32_16x16x128_f8f6f4 v[0:3], v[236:243], v[220:227], v[0:3]
	s_setprio 0
	s_barrier
	s_add_u32 s36, s36, 0x40080
	s_addc_u32 s37, s37, 0
	s_mov_b32 m0, s52
	v_lshl_add_u64 v[144:145], s[36:37], 0, v[128:129]
	global_load_lds_dwordx4 v[144:145], off
	v_lshl_add_u64 v[144:145], s[36:37], 0, v[130:131]
	s_mov_b32 m0, s53
	s_add_i32 s59, s59, 2
	global_load_lds_dwordx4 v[144:145], off
	s_add_u32 s34, s34, 0x100
	s_addc_u32 s35, s35, 0
	s_cmp_gt_u32 s59, 13
	s_cbranch_scc0 .LBB0_1503
	s_and_b64 vcc, exec, s[20:21]
	s_cbranch_vccz .LBB0_1506
	s_barrier
